# phase 8 pass 1: second row's 8 loads issued together with the first row's (spare registers, copied in place later); on top of v42
# baseline (speedup 1.0000x reference)
; #define GAS __attribute__((address_space(1)))
; __device__ __forceinline__ float dot4(f32x4 a, f32x4 b) { return (a.x * b.x + a.y * b.y) + (a.z * b.z + a.w * b.w); }
; __device__ __forceinline__ void phase8(KP kp, LAS unsigned char* lds, int wave, int bid) {
;     ...
;     for (int q = 0; q < 4; ++q) {
;         const int lt = 4 * wave + q, t = 32 * bid + lt;
;         const GAS f32x4* xr = (const GAS f32x4*)(X1 + (size_t)t * DM) + lane;
;         f32x4 v[8]; float s = 0.f;
; #pragma unroll
;         for (int j = 0; j < 8; ++j) { v[j] = xr[64 * j]; s += dot4(v[j], v[j]); }
;         const float rstd = 1.0f / sqrtf(wave_sum(s) * (1.0f / DM) + EPS);
;         if (lane == 0) rs[lt] = rstd;
.LBB0_933:
	v_lshl_add_u64 v[42:43], s[8:9], 0, v[38:39]
	v_add_co_u32_e32 v16, vcc, s20, v42
	s_nop 1
	v_addc_co_u32_e32 v17, vcc, 0, v43, vcc
	global_load_dwordx4 v[12:15], v[16:17], off
	v_add_co_u32_e32 v40, vcc, 0x56000000, v42
	global_load_dwordx4 v[8:11], v[16:17], off offset:1024
	global_load_dwordx4 v[4:7], v[16:17], off offset:2048
	global_load_dwordx4 v[0:3], v[16:17], off offset:3072
	v_addc_co_u32_e32 v41, vcc, 0, v43, vcc
	global_load_dwordx4 v[28:31], v[40:41], off
	global_load_dwordx4 v[24:27], v[40:41], off offset:1024
	global_load_dwordx4 v[20:23], v[40:41], off offset:2048
	global_load_dwordx4 v[16:19], v[40:41], off offset:3072
	v_add_co_u32_e32 v192, vcc, s28, v42
	s_nop 1
	v_addc_co_u32_e32 v193, vcc, 0, v43, vcc
	v_add_co_u32_e32 v194, vcc, s25, v42
	s_nop 1
	v_addc_co_u32_e32 v195, vcc, 0, v43, vcc
	global_load_dwordx4 v[188:191], v[192:193], off offset:-4096
	global_load_dwordx4 v[184:187], v[194:195], off offset:1024
	global_load_dwordx4 v[180:183], v[194:195], off offset:2048
	global_load_dwordx4 v[176:179], v[194:195], off offset:3072
	global_load_dwordx4 v[172:175], v[192:193], off
	global_load_dwordx4 v[168:171], v[192:193], off offset:1024
	global_load_dwordx4 v[164:167], v[192:193], off offset:2048
	global_load_dwordx4 v[160:163], v[192:193], off offset:3072
	s_waitcnt vmcnt(15)
	v_mul_f32_e32 v40, v13, v13
	v_mul_f32_e32 v41, v15, v15
	s_waitcnt vmcnt(14)
	v_mul_f32_e32 v44, v9, v9
	v_mul_f32_e32 v52, v11, v11
	s_waitcnt vmcnt(13)
	v_mul_f32_e32 v53, v5, v5
	v_mul_f32_e32 v54, v7, v7
	s_waitcnt vmcnt(11)
	v_mul_f32_e32 v57, v29, v29
	v_mul_f32_e32 v58, v31, v31
	s_waitcnt vmcnt(10)
	v_mul_f32_e32 v59, v25, v25
	v_mul_f32_e32 v60, v27, v27
	v_mul_f32_e32 v55, v1, v1
	v_mul_f32_e32 v56, v3, v3
	s_waitcnt vmcnt(9)
	v_mul_f32_e32 v61, v21, v21
	v_mul_f32_e32 v62, v23, v23
	v_fmac_f32_e32 v40, v12, v12
	v_fmac_f32_e32 v41, v14, v14
	v_fmac_f32_e32 v44, v8, v8
	v_fmac_f32_e32 v52, v10, v10
	v_fmac_f32_e32 v53, v4, v4
	v_fmac_f32_e32 v54, v6, v6
	v_fmac_f32_e32 v57, v28, v28
	v_fmac_f32_e32 v58, v30, v30
	v_fmac_f32_e32 v59, v24, v24
	v_fmac_f32_e32 v60, v26, v26
	s_waitcnt vmcnt(8)
	v_mul_f32_e32 v63, v17, v17
	v_mul_f32_e32 v64, v19, v19
	v_fmac_f32_e32 v55, v0, v0
	v_fmac_f32_e32 v56, v2, v2
	v_fmac_f32_e32 v61, v20, v20
	v_fmac_f32_e32 v62, v22, v22
	v_add_f32_e32 v40, v40, v41
	v_add_f32_e32 v41, v44, v52
	v_add_f32_e32 v44, v53, v54
	v_add_f32_e32 v53, v57, v58
	v_add_f32_e32 v54, v59, v60
	v_fmac_f32_e32 v63, v16, v16
	v_fmac_f32_e32 v64, v18, v18
	v_add_f32_e32 v52, v55, v56
	v_add_f32_e32 v55, v61, v62
	v_add_f32_e32 v53, v53, v54
	v_add_f32_e32 v56, v63, v64
	v_add_f32_e32 v53, v53, v55
	v_add_f32_e32 v53, v53, v56
	v_add_f32_e32 v40, v53, v40
	v_add_f32_e32 v40, v40, v41
	v_add_f32_e32 v40, v40, v44
	v_add_f32_e32 v40, v40, v52
	s_nop 1
	v_add_f32_dpp v40, v40, v40 quad_perm:[1,0,3,2] row_mask:0xf bank_mask:0xf
	s_nop 1
	v_add_f32_dpp v40, v40, v40 quad_perm:[2,3,0,1] row_mask:0xf bank_mask:0xf
	s_nop 1
	v_add_f32_dpp v40, v40, v40 row_half_mirror row_mask:0xf bank_mask:0xf
	s_nop 1
	v_add_f32_dpp v40, v40, v40 row_mirror row_mask:0xf bank_mask:0xf
	v_mov_b32_e32 v41, v40
	s_nop 1
	v_permlane16_swap_b32_e32 v40, v41
	v_add_f32_e32 v40, v40, v41
	v_mov_b32_e32 v41, v40
	s_nop 1
	v_permlane32_swap_b32_e32 v40, v41
	v_add_f32_e32 v40, v40, v41
	v_fmamk_f32 v40, v40, 0x3a000000, v35
	v_mul_f32_e32 v41, 0x4f800000, v40
	v_cmp_gt_f32_e32 vcc, s21, v40
	s_nop 1
	v_cndmask_b32_e32 v40, v40, v41, vcc
	v_sqrt_f32_e32 v41, v40
	s_nop 0
	v_add_u32_e32 v44, -1, v41
	v_add_u32_e32 v52, 1, v41
	v_fma_f32 v53, -v44, v41, v40
	v_fma_f32 v54, -v52, v41, v40
	v_cmp_ge_f32_e64 s[6:7], 0, v53
	s_nop 1
	v_cndmask_b32_e64 v41, v41, v44, s[6:7]
	v_cmp_lt_f32_e64 s[6:7], 0, v54
	s_nop 1
	v_cndmask_b32_e64 v41, v41, v52, s[6:7]
	v_mul_f32_e32 v44, 0x37800000, v41
	v_cndmask_b32_e32 v41, v41, v44, vcc
	v_cmp_class_f32_e32 vcc, v40, v51
	s_nop 1
	v_cndmask_b32_e32 v40, v41, v40, vcc
	v_div_scale_f32 v41, s[6:7], v40, v40, 1.0
	v_rcp_f32_e32 v44, v41
	v_div_scale_f32 v52, vcc, 1.0, v40, 1.0
	v_fma_f32 v53, -v41, v44, 1.0
	v_fmac_f32_e32 v44, v53, v44
	v_mul_f32_e32 v53, v52, v44
	v_fma_f32 v54, -v41, v53, v52
	v_fmac_f32_e32 v53, v54, v44
	v_fma_f32 v41, -v41, v53, v52
	v_div_fmas_f32 v41, v41, v44, v53
	v_div_fixup_f32 v44, v41, v40, 1.0
	s_and_saveexec_b64 s[6:7], s[2:3]
	s_add_i32 s4, s5, s18
	v_mov_b32_e32 v40, s4
	ds_write_b32 v40, v44
	s_or_b64 exec, exec, s[6:7]
	ds_read_b128 v[52:55], v50
	ds_read_b128 v[56:59], v50 offset:8192
	v_pk_mul_f32 v[64:65], v[30:31], v[44:45] op_sel_hi:[1,0]
	v_pk_mul_f32 v[66:67], v[28:29], v[44:45] op_sel_hi:[1,0]
	ds_read_b128 v[28:31], v50 offset:1024
	ds_read_b128 v[60:63], v50 offset:9216
	v_pk_mul_f32 v[24:25], v[24:25], v[44:45] op_sel_hi:[1,0]
	s_waitcnt lgkmcnt(2)
	v_pk_fma_f32 v[52:53], v[66:67], v[52:53], v[56:57]
	v_pk_mul_f32 v[26:27], v[26:27], v[44:45] op_sel_hi:[1,0]
	v_bfe_u32 v56, v52, 16, 1
	s_waitcnt lgkmcnt(0)
; #define GAS __attribute__((address_space(1)))
; #define LAS __attribute__((address_space(3)))
; __device__ __forceinline__ u32x2 pack4(f32x4 v) { u32x2 w; w.x = pk2(v.x, v.y); w.y = pk2(v.z, v.w); return w; }
; __device__ __forceinline__ void phase8(KP kp, LAS unsigned char* lds, int wave, int bid) {
;     ...
;         GAS u32x2* o8 = (GAS u32x2*)(H + (size_t)t * DM) + lane;
; #pragma unroll
;         for (int j = 0; j < 8; ++j) { const f32x4 av = *(const LAS f32x4*)(A2 + 256 * j + 4 * lane), bv = *(const LAS f32x4*)(B2 + 256 * j + 4 * lane);
;             o8[64 * j] = pack4(v[j] * rstd * av + bv); }
	v_pk_fma_f32 v[24:25], v[24:25], v[28:29], v[60:61]
	v_add3_u32 v52, v52, v56, s22
	v_bfe_u32 v28, v24, 16, 1
	v_bfe_u32 v56, v53, 16, 1
	v_add3_u32 v24, v24, v28, s22
	v_bfe_u32 v28, v25, 16, 1
	v_pk_fma_f32 v[54:55], v[64:65], v[54:55], v[58:59]
	v_lshrrev_b32_e32 v52, 16, v52
	v_add3_u32 v53, v53, v56, s22
	v_pk_fma_f32 v[26:27], v[26:27], v[30:31], v[62:63]
	v_lshrrev_b32_e32 v24, 16, v24
	v_add3_u32 v25, v25, v28, s22
	v_and_or_b32 v52, v53, s23, v52
	v_bfe_u32 v53, v54, 16, 1
	v_and_or_b32 v24, v25, s23, v24
	v_bfe_u32 v25, v26, 16, 1
	v_lshl_add_u64 v[40:41], s[8:9], 0, v[36:37]
	v_add3_u32 v53, v54, v53, s22
	v_bfe_u32 v54, v55, 16, 1
	v_add3_u32 v25, v26, v25, s22
	v_bfe_u32 v26, v27, 16, 1
	v_lshrrev_b32_e32 v53, 16, v53
	v_add3_u32 v54, v55, v54, s22
	v_add_co_u32_e32 v56, vcc, s24, v40
	v_lshrrev_b32_e32 v25, 16, v25
	v_add3_u32 v26, v27, v26, s22
	v_and_or_b32 v53, v54, s23, v53
	v_addc_co_u32_e32 v57, vcc, 0, v41, vcc
	v_and_or_b32 v25, v26, s23, v25
	global_store_dwordx2 v[56:57], v[52:53], off
	global_store_dwordx2 v[56:57], v[24:25], off offset:512
	ds_read_b128 v[24:27], v50 offset:2048
	ds_read_b128 v[28:31], v50 offset:10240
	v_pk_mul_f32 v[58:59], v[22:23], v[44:45] op_sel_hi:[1,0]
	v_pk_mul_f32 v[60:61], v[20:21], v[44:45] op_sel_hi:[1,0]
	ds_read_b128 v[20:23], v50 offset:3072
	ds_read_b128 v[52:55], v50 offset:11264
	v_pk_mul_f32 v[16:17], v[16:17], v[44:45] op_sel_hi:[1,0]
	s_waitcnt lgkmcnt(2)
	v_pk_fma_f32 v[24:25], v[60:61], v[24:25], v[28:29]
	v_pk_mul_f32 v[18:19], v[18:19], v[44:45] op_sel_hi:[1,0]
	v_bfe_u32 v28, v24, 16, 1
	s_waitcnt lgkmcnt(0)
	v_pk_fma_f32 v[16:17], v[16:17], v[20:21], v[52:53]
	v_add3_u32 v24, v24, v28, s22
	v_bfe_u32 v20, v16, 16, 1
	v_bfe_u32 v28, v25, 16, 1
	v_add3_u32 v16, v16, v20, s22
	v_bfe_u32 v20, v17, 16, 1
	v_pk_fma_f32 v[26:27], v[58:59], v[26:27], v[30:31]
	v_lshrrev_b32_e32 v24, 16, v24
	v_add3_u32 v25, v25, v28, s22
	v_pk_fma_f32 v[18:19], v[18:19], v[22:23], v[54:55]
	v_lshrrev_b32_e32 v16, 16, v16
	v_add3_u32 v17, v17, v20, s22
	v_and_or_b32 v24, v25, s23, v24
	v_bfe_u32 v25, v26, 16, 1
	v_and_or_b32 v16, v17, s23, v16
	v_bfe_u32 v17, v18, 16, 1
	v_add3_u32 v25, v26, v25, s22
	v_bfe_u32 v26, v27, 16, 1
	v_add3_u32 v17, v18, v17, s22
	v_bfe_u32 v18, v19, 16, 1
	v_lshrrev_b32_e32 v25, 16, v25
	v_add3_u32 v26, v27, v26, s22
	v_lshrrev_b32_e32 v17, 16, v17
	v_add3_u32 v18, v19, v18, s22
	v_and_or_b32 v25, v26, s23, v25
	v_and_or_b32 v17, v18, s23, v17
	global_store_dwordx2 v[56:57], v[24:25], off offset:1024
	global_store_dwordx2 v[56:57], v[16:17], off offset:1536
	ds_read_b128 v[16:19], v50 offset:4096
	ds_read_b128 v[20:23], v50 offset:12288
	v_pk_mul_f32 v[28:29], v[14:15], v[44:45] op_sel_hi:[1,0]
	v_pk_mul_f32 v[30:31], v[12:13], v[44:45] op_sel_hi:[1,0]
	ds_read_b128 v[12:15], v50 offset:5120
	ds_read_b128 v[24:27], v50 offset:13312
	v_pk_mul_f32 v[8:9], v[8:9], v[44:45] op_sel_hi:[1,0]
	s_waitcnt lgkmcnt(2)
	v_pk_fma_f32 v[16:17], v[30:31], v[16:17], v[20:21]
	v_pk_mul_f32 v[10:11], v[10:11], v[44:45] op_sel_hi:[1,0]
	v_bfe_u32 v20, v16, 16, 1
	s_waitcnt lgkmcnt(0)
	v_pk_fma_f32 v[8:9], v[8:9], v[12:13], v[24:25]
	v_add3_u32 v16, v16, v20, s22
	v_bfe_u32 v12, v8, 16, 1
	v_bfe_u32 v20, v17, 16, 1
	v_add3_u32 v8, v8, v12, s22
	v_bfe_u32 v12, v9, 16, 1
	v_pk_fma_f32 v[18:19], v[28:29], v[18:19], v[22:23]
	v_lshrrev_b32_e32 v16, 16, v16
	v_add3_u32 v17, v17, v20, s22
	v_pk_fma_f32 v[10:11], v[10:11], v[14:15], v[26:27]
	v_lshrrev_b32_e32 v8, 16, v8
	v_add3_u32 v9, v9, v12, s22
	v_and_or_b32 v16, v17, s23, v16
	v_bfe_u32 v17, v18, 16, 1
	v_and_or_b32 v8, v9, s23, v8
	v_bfe_u32 v9, v10, 16, 1
	v_add3_u32 v17, v18, v17, s22
	v_bfe_u32 v18, v19, 16, 1
	v_add3_u32 v9, v10, v9, s22
	v_bfe_u32 v10, v11, 16, 1
	v_lshrrev_b32_e32 v17, 16, v17
	v_add3_u32 v18, v19, v18, s22
	v_lshrrev_b32_e32 v9, 16, v9
	v_add3_u32 v10, v11, v10, s22
	v_and_or_b32 v17, v18, s23, v17
	v_and_or_b32 v9, v10, s23, v9
	global_store_dwordx2 v[56:57], v[16:17], off offset:2048
	global_store_dwordx2 v[56:57], v[8:9], off offset:2560
	ds_read_b128 v[8:11], v50 offset:6144
	ds_read_b128 v[12:15], v50 offset:14336
	v_pk_mul_f32 v[20:21], v[6:7], v[44:45] op_sel_hi:[1,0]
	v_pk_mul_f32 v[22:23], v[4:5], v[44:45] op_sel_hi:[1,0]
	ds_read_b128 v[4:7], v50 offset:7168
	ds_read_b128 v[16:19], v50 offset:15360
	v_pk_mul_f32 v[0:1], v[0:1], v[44:45] op_sel_hi:[1,0]
	s_waitcnt lgkmcnt(2)
	v_pk_fma_f32 v[8:9], v[22:23], v[8:9], v[12:13]
	v_pk_mul_f32 v[2:3], v[2:3], v[44:45] op_sel_hi:[1,0]
	v_bfe_u32 v12, v8, 16, 1
	s_waitcnt lgkmcnt(0)
; #define GAS __attribute__((address_space(1)))
; __device__ __forceinline__ float dot4(f32x4 a, f32x4 b) { return (a.x * b.x + a.y * b.y) + (a.z * b.z + a.w * b.w); }
; __device__ __forceinline__ void phase8(KP kp, LAS unsigned char* lds, int wave, int bid) {
;     ...
;         const int lt = 4 * wave + q, t = 32 * bid + lt;
;         const GAS f32x4* xr = (const GAS f32x4*)(X1 + (size_t)t * DM) + lane;
;         f32x4 v[8]; float s = 0.f;
; #pragma unroll
;         for (int j = 0; j < 8; ++j) { v[j] = xr[64 * j]; s += dot4(v[j], v[j]); }
;         const float rstd = 1.0f / sqrtf(wave_sum(s) * (1.0f / DM) + EPS);
;         if (lane == 0) rs[lt] = rstd;
	v_pk_fma_f32 v[0:1], v[0:1], v[4:5], v[16:17]
	v_add3_u32 v8, v8, v12, s22
	v_bfe_u32 v4, v0, 16, 1
	v_bfe_u32 v12, v9, 16, 1
	v_add3_u32 v0, v0, v4, s22
	v_bfe_u32 v4, v1, 16, 1
	v_pk_fma_f32 v[10:11], v[20:21], v[10:11], v[14:15]
	v_lshrrev_b32_e32 v8, 16, v8
	v_add3_u32 v9, v9, v12, s22
	v_pk_fma_f32 v[2:3], v[2:3], v[6:7], v[18:19]
	v_lshrrev_b32_e32 v0, 16, v0
	v_add3_u32 v1, v1, v4, s22
	v_and_or_b32 v8, v9, s23, v8
	v_bfe_u32 v9, v10, 16, 1
	v_and_or_b32 v0, v1, s23, v0
	v_bfe_u32 v1, v2, 16, 1
	v_add3_u32 v9, v10, v9, s22
	v_bfe_u32 v10, v11, 16, 1
	v_add3_u32 v1, v2, v1, s22
	v_bfe_u32 v2, v3, 16, 1
	v_lshrrev_b32_e32 v9, 16, v9
	v_add3_u32 v10, v11, v10, s22
	v_lshrrev_b32_e32 v1, 16, v1
	v_add3_u32 v2, v3, v2, s22
	v_and_or_b32 v9, v10, s23, v9
	v_and_or_b32 v1, v2, s23, v1
	v_add_co_u32_e32 v52, vcc, s28, v42
	global_store_dwordx2 v[56:57], v[8:9], off offset:3072
	global_store_dwordx2 v[56:57], v[0:1], off offset:3584
	v_addc_co_u32_e32 v53, vcc, 0, v43, vcc
	v_add_co_u32_e32 v42, vcc, s25, v42
	s_nop 1
	v_addc_co_u32_e32 v43, vcc, 0, v43, vcc
	s_waitcnt vmcnt(8)
	s_nop 1
	v_mov_b32_e32 v0, v160
	v_mov_b32_e32 v1, v161
	v_mov_b32_e32 v2, v162
	v_mov_b32_e32 v3, v163
	v_mov_b32_e32 v4, v164
	v_mov_b32_e32 v5, v165
	v_mov_b32_e32 v6, v166
	v_mov_b32_e32 v7, v167
	v_mov_b32_e32 v8, v168
	v_mov_b32_e32 v9, v169
	v_mov_b32_e32 v10, v170
	v_mov_b32_e32 v11, v171
	v_mov_b32_e32 v12, v172
	v_mov_b32_e32 v13, v173
	v_mov_b32_e32 v14, v174
	v_mov_b32_e32 v15, v175
	v_mov_b32_e32 v16, v176
	v_mov_b32_e32 v17, v177
	v_mov_b32_e32 v18, v178
	v_mov_b32_e32 v19, v179
	v_mov_b32_e32 v20, v180
	v_mov_b32_e32 v21, v181
	v_mov_b32_e32 v22, v182
	v_mov_b32_e32 v23, v183
	v_mov_b32_e32 v24, v184
	v_mov_b32_e32 v25, v185
	v_mov_b32_e32 v26, v186
	v_mov_b32_e32 v27, v187
	v_mov_b32_e32 v28, v188
	v_mov_b32_e32 v29, v189
	v_mov_b32_e32 v30, v190
	v_mov_b32_e32 v31, v191
	v_mul_f32_e32 v42, v29, v29
	v_mul_f32_e32 v43, v31, v31
	v_fmac_f32_e32 v42, v28, v28
	v_fmac_f32_e32 v43, v30, v30
	v_add_f32_e32 v42, v42, v43
	v_mul_f32_e32 v43, v25, v25
	v_mul_f32_e32 v44, v27, v27
	v_fmac_f32_e32 v43, v24, v24
	v_fmac_f32_e32 v44, v26, v26
	v_add_f32_e32 v43, v43, v44
	v_add_f32_e32 v42, v42, v43
	v_mul_f32_e32 v43, v21, v21
	v_mul_f32_e32 v44, v23, v23
	v_fmac_f32_e32 v43, v20, v20
	v_fmac_f32_e32 v44, v22, v22
	v_add_f32_e32 v43, v43, v44
	v_add_f32_e32 v42, v42, v43
	v_mul_f32_e32 v43, v17, v17
	v_mul_f32_e32 v44, v19, v19
	v_fmac_f32_e32 v43, v16, v16
	v_fmac_f32_e32 v44, v18, v18
	v_add_f32_e32 v43, v43, v44
	v_add_f32_e32 v42, v42, v43
	v_mul_f32_e32 v43, v13, v13
	v_mul_f32_e32 v44, v15, v15
	v_fmac_f32_e32 v43, v12, v12
	v_fmac_f32_e32 v44, v14, v14
	v_add_f32_e32 v43, v43, v44
	v_add_f32_e32 v42, v42, v43
	v_mul_f32_e32 v43, v9, v9
	v_mul_f32_e32 v44, v11, v11
	v_fmac_f32_e32 v43, v8, v8
	v_fmac_f32_e32 v44, v10, v10
	v_add_f32_e32 v43, v43, v44
	v_add_f32_e32 v42, v42, v43
	v_mul_f32_e32 v43, v5, v5
	v_mul_f32_e32 v44, v7, v7
	v_fmac_f32_e32 v43, v4, v4
	v_fmac_f32_e32 v44, v6, v6
	v_add_f32_e32 v43, v43, v44
	v_add_f32_e32 v42, v42, v43
	v_mul_f32_e32 v43, v1, v1
	v_mul_f32_e32 v44, v3, v3
	v_fmac_f32_e32 v43, v0, v0
	v_fmac_f32_e32 v44, v2, v2
	v_add_f32_e32 v43, v43, v44
	v_add_f32_e32 v42, v42, v43
	s_nop 1
	v_add_f32_dpp v42, v42, v42 quad_perm:[1,0,3,2] row_mask:0xf bank_mask:0xf
	s_nop 1
	v_add_f32_dpp v42, v42, v42 quad_perm:[2,3,0,1] row_mask:0xf bank_mask:0xf
	s_nop 1
	v_add_f32_dpp v42, v42, v42 row_half_mirror row_mask:0xf bank_mask:0xf
	s_nop 1
	v_add_f32_dpp v42, v42, v42 row_mirror row_mask:0xf bank_mask:0xf
	v_mov_b32_e32 v43, v42
	s_nop 1
	v_permlane16_swap_b32_e32 v42, v43
	v_add_f32_e32 v42, v42, v43
	v_mov_b32_e32 v43, v42
	s_nop 1
	v_permlane32_swap_b32_e32 v42, v43
	v_add_f32_e32 v42, v42, v43
	v_fmamk_f32 v42, v42, 0x3a000000, v35
	v_mul_f32_e32 v43, 0x4f800000, v42
	v_cmp_gt_f32_e32 vcc, s21, v42
	s_nop 1
	v_cndmask_b32_e32 v42, v42, v43, vcc
	v_sqrt_f32_e32 v43, v42
	s_nop 0
	v_add_u32_e32 v44, -1, v43
	v_fma_f32 v52, -v44, v43, v42
	v_cmp_ge_f32_e64 s[6:7], 0, v52
	v_add_u32_e32 v52, 1, v43
	s_nop 0
	v_cndmask_b32_e64 v44, v43, v44, s[6:7]
	v_fma_f32 v43, -v52, v43, v42
	v_cmp_lt_f32_e64 s[6:7], 0, v43
	s_nop 1
	v_cndmask_b32_e64 v43, v44, v52, s[6:7]
	v_mul_f32_e32 v44, 0x37800000, v43
	v_cndmask_b32_e32 v43, v43, v44, vcc
	v_cmp_class_f32_e32 vcc, v42, v51
	s_nop 1
	v_cndmask_b32_e32 v42, v43, v42, vcc
	v_div_scale_f32 v43, s[6:7], v42, v42, 1.0
	v_rcp_f32_e32 v44, v43
	s_nop 0
	v_fma_f32 v52, -v43, v44, 1.0
	v_fmac_f32_e32 v44, v52, v44
	v_div_scale_f32 v52, vcc, 1.0, v42, 1.0
	v_mul_f32_e32 v53, v52, v44
	v_fma_f32 v54, -v43, v53, v52
	v_fmac_f32_e32 v53, v54, v44
	v_fma_f32 v43, -v43, v53, v52
	v_div_fmas_f32 v43, v43, v44, v53
	v_div_fixup_f32 v42, v43, v42, 1.0
	s_and_saveexec_b64 s[6:7], s[2:3]
	s_cbranch_execz .LBB0_932
	s_add_i32 s4, s5, s18
	v_mov_b32_e32 v43, s4
	ds_write_b32 v43, v42 offset:4
	s_branch .LBB0_932
